# MLA loop: software-pipelined LDS reads (8-deep ring for K fragments in QK, V fragments pre-issued before softmax and ring in PV)
# speedup vs baseline: 1.0030x; 1.0020x over previous
; #define LAS __attribute__((address_space(3)))
; #define AT_MFMA(a, b, c) __builtin_amdgcn_mfma_f32_32x32x16_bf16((a), (b), (c), 0, 0, 0)
; template <bool MLA>
; __device__ __forceinline__ void attn_unit(const P& p, LAS unsigned char* lds, const int b, const int h, const int qb) {
;     ...
;             for (int s = 0; s < NQF; ++s) { const bf16x8 a0 = *(const LAS bf16x8*)(kb + r32 * KSTR + s * 32 + hi * 16), a1 = *(const LAS bf16x8*)(kb + (32 + r32) * KSTR + s * 32 + hi * 16);
;                 p0 = AT_MFMA(a0, qf[s], p0); p1 = AT_MFMA(a1, qf[s], p1); if ((s & 3) == 3) __builtin_amdgcn_sched_barrier(0); }
;     ...
;             for (int d0 = 0; d0 < 4; ++d0) { const LAS unsigned char* vr = vb + (32 * d0 + r32) * VSTR + hi * 16;
;                 o[d0] = AT_MFMA(pf0, *(const LAS bf16x8*)(vr), o[d0]); o[d0] = AT_MFMA(pf1, *(const LAS bf16x8*)(vr + 32), o[d0]);
;                 o[d0] = AT_MFMA(pf2, *(const LAS bf16x8*)(vr + 64), o[d0]); o[d0] = AT_MFMA(pf3, *(const LAS bf16x8*)(vr + 96), o[d0]); __builtin_amdgcn_sched_barrier(0); }
.LBB0_708:
	s_and_b32 s95, s0, 1
	s_sub_i32 s0, s84, 64
	s_cmp_gt_u32 s0, s93
	s_cbranch_scc1 .LBB0_716
	s_mul_i32 s0, s95, 0xac00
	s_add_i32 s96, s0, 0
	v_add3_u32 v3, s96, v202, v198
	ds_read_b128 v[4:7], v3
	ds_read_b128 v[8:11], v3 offset:12800
	ds_read_b128 v[12:15], v3 offset:32
	ds_read_b128 v[228:231], v3 offset:12832
	ds_read_b128 v[232:235], v3 offset:64
	ds_read_b128 v[236:239], v3 offset:12864
	ds_read_b128 v[244:247], v3 offset:96
	ds_read_b128 v[248:251], v3 offset:12896
	s_waitcnt lgkmcnt(7)
	v_mfma_f32_32x32x16_bf16 v[82:97], v[4:7], v[134:137], 0
	ds_read_b128 v[252:255], v3 offset:128
	s_waitcnt lgkmcnt(7)
	v_mfma_f32_32x32x16_bf16 v[98:113], v[8:11], v[134:137], 0
	ds_read_b128 v[4:7], v3 offset:12928
	s_waitcnt lgkmcnt(7)
	v_mfma_f32_32x32x16_bf16 v[82:97], v[12:15], v[114:117], v[82:97]
	ds_read_b128 v[8:11], v3 offset:160
	s_waitcnt lgkmcnt(7)
	v_mfma_f32_32x32x16_bf16 v[98:113], v[228:231], v[114:117], v[98:113]
	ds_read_b128 v[12:15], v3 offset:12960
	s_waitcnt lgkmcnt(7)
	v_mfma_f32_32x32x16_bf16 v[82:97], v[232:235], v[118:121], v[82:97]
	ds_read_b128 v[228:231], v3 offset:192
	s_waitcnt lgkmcnt(7)
	v_mfma_f32_32x32x16_bf16 v[98:113], v[236:239], v[118:121], v[98:113]
	ds_read_b128 v[232:235], v3 offset:12992
	s_waitcnt lgkmcnt(7)
	v_mfma_f32_32x32x16_bf16 v[82:97], v[244:247], v[122:125], v[82:97]
	ds_read_b128 v[236:239], v3 offset:224
	s_waitcnt lgkmcnt(7)
	v_mfma_f32_32x32x16_bf16 v[98:113], v[248:251], v[122:125], v[98:113]
	ds_read_b128 v[244:247], v3 offset:13024
	s_waitcnt lgkmcnt(7)
	v_mfma_f32_32x32x16_bf16 v[82:97], v[252:255], v[126:129], v[82:97]
	ds_read_b128 v[248:251], v3 offset:256
	s_waitcnt lgkmcnt(7)
	v_mfma_f32_32x32x16_bf16 v[98:113], v[4:7], v[126:129], v[98:113]
	ds_read_b128 v[252:255], v3 offset:13056
	s_waitcnt lgkmcnt(7)
	v_mfma_f32_32x32x16_bf16 v[82:97], v[8:11], v[146:149], v[82:97]
	ds_read_b128 v[4:7], v3 offset:288
	s_waitcnt lgkmcnt(7)
	v_mfma_f32_32x32x16_bf16 v[98:113], v[12:15], v[146:149], v[98:113]
	ds_read_b128 v[8:11], v3 offset:13088
	s_waitcnt lgkmcnt(7)
	v_mfma_f32_32x32x16_bf16 v[82:97], v[228:231], v[150:153], v[82:97]
	ds_read_b128 v[12:15], v3 offset:320
	s_waitcnt lgkmcnt(7)
	v_mfma_f32_32x32x16_bf16 v[98:113], v[232:235], v[150:153], v[98:113]
	ds_read_b128 v[228:231], v3 offset:13120
	s_waitcnt lgkmcnt(7)
	v_mfma_f32_32x32x16_bf16 v[82:97], v[236:239], v[154:157], v[82:97]
	ds_read_b128 v[232:235], v3 offset:352
	s_waitcnt lgkmcnt(7)
	v_mfma_f32_32x32x16_bf16 v[98:113], v[244:247], v[154:157], v[98:113]
	ds_read_b128 v[236:239], v3 offset:13152
	s_waitcnt lgkmcnt(7)
	v_mfma_f32_32x32x16_bf16 v[82:97], v[248:251], v[158:161], v[82:97]
	s_waitcnt lgkmcnt(6)
	v_mfma_f32_32x32x16_bf16 v[98:113], v[252:255], v[158:161], v[98:113]
	s_waitcnt lgkmcnt(5)
	v_mfma_f32_32x32x16_bf16 v[82:97], v[4:7], v[162:165], v[82:97]
	s_waitcnt lgkmcnt(4)
	v_mfma_f32_32x32x16_bf16 v[98:113], v[8:11], v[162:165], v[98:113]
	s_waitcnt lgkmcnt(3)
	v_mfma_f32_32x32x16_bf16 v[82:97], v[12:15], v[166:169], v[82:97]
	s_waitcnt lgkmcnt(2)
	v_mfma_f32_32x32x16_bf16 v[98:113], v[228:231], v[166:169], v[98:113]
	s_waitcnt lgkmcnt(1)
	v_mfma_f32_32x32x16_bf16 v[82:97], v[232:235], v[130:133], v[82:97]
	s_waitcnt lgkmcnt(0)
	v_mfma_f32_32x32x16_bf16 v[98:113], v[236:239], v[130:133], v[98:113]
	v_add3_u32 v243, s96, v198, v204
	ds_read_b128 v[228:231], v243 offset:25600
	ds_read_b128 v[232:235], v243 offset:25632
	ds_read_b128 v[236:239], v243 offset:25664
	ds_read_b128 v[244:247], v243 offset:25696
	ds_read_b128 v[248:251], v243 offset:30208
	ds_read_b128 v[252:255], v243 offset:30240
	s_add_i32 s0, s84, -1
	s_cmp_le_u32 s0, s2
	s_cbranch_scc1 .LBB0_711
; template <bool MLA>
; __device__ __forceinline__ void attn_unit(const P& p, LAS unsigned char* lds, const int b, const int h, const int qb) {
;     ...
;                 if (k0 + 63 > qw) {
; #pragma unroll
;                     for (int r = 0; r < 16; ++r) { const int c = (r & 3) + 8 * (r >> 2);
;                         if (c > dq) p0[r] = -__builtin_inff(); if (c + 32 > dq) p1[r] = -__builtin_inff(); }
	v_cmp_gt_i32_e64 s[66:67], 26, v213
	v_cmp_gt_i32_e64 s[68:69], 27, v213
	v_cmp_gt_i32_e64 s[64:65], 25, v213
	s_and_b64 s[66:67], s[68:69], s[66:67]
	v_cmp_gt_i32_e64 s[62:63], 24, v213
	s_and_b64 s[64:65], s[66:67], s[64:65]
	v_cmp_gt_i32_e64 s[60:61], 19, v213
	s_and_b64 s[62:63], s[64:65], s[62:63]
	v_cmp_gt_i32_e64 s[58:59], 18, v213
	s_and_b64 s[60:61], s[62:63], s[60:61]
	v_cmp_gt_i32_e64 s[56:57], 17, v213
	s_and_b64 s[58:59], s[60:61], s[58:59]
	v_cmp_gt_i32_e64 s[54:55], 16, v213
	s_and_b64 s[56:57], s[58:59], s[56:57]
	v_cmp_gt_i32_e64 s[52:53], 11, v213
	s_and_b64 s[54:55], s[56:57], s[54:55]
	v_cmp_gt_i32_e64 s[50:51], 10, v213
	s_and_b64 s[52:53], s[54:55], s[52:53]
	v_cmp_gt_i32_e64 s[48:49], 9, v213
	s_and_b64 s[50:51], s[52:53], s[50:51]
	v_cmp_gt_i32_e64 s[46:47], 8, v213
	s_and_b64 s[48:49], s[50:51], s[48:49]
	v_cmp_gt_i32_e64 s[44:45], 3, v213
	s_and_b64 s[46:47], s[48:49], s[46:47]
	v_cmp_gt_i32_e64 s[42:43], 2, v213
	s_and_b64 s[44:45], s[46:47], s[44:45]
	v_cmp_gt_i32_e64 s[38:39], 1, v213
	s_and_b64 s[42:43], s[44:45], s[42:43]
	v_cmp_gt_i32_e64 s[0:1], 0, v213
	s_and_b64 s[38:39], s[42:43], s[38:39]
	s_and_b64 s[0:1], s[38:39], s[0:1]
	v_cmp_gt_i32_e64 s[36:37], 58, v213
	v_cndmask_b32_e64 v82, v82, v210, s[0:1]
	v_cmp_gt_i32_e64 s[0:1], 59, v213
	v_cmp_gt_i32_e64 s[34:35], 57, v213
	v_cmp_gt_i32_e64 s[30:31], 56, v213
	v_cndmask_b32_e64 v113, v113, v210, s[0:1]
	s_and_b64 s[0:1], s[0:1], s[36:37]
	v_cndmask_b32_e64 v112, v112, v210, s[0:1]
	s_and_b64 s[0:1], s[0:1], s[34:35]
	v_cmp_gt_i32_e64 s[28:29], 51, v213
	v_cndmask_b32_e64 v111, v111, v210, s[0:1]
	s_and_b64 s[0:1], s[0:1], s[30:31]
	v_cmp_gt_i32_e64 s[26:27], 50, v213
	v_cndmask_b32_e64 v110, v110, v210, s[0:1]
	s_and_b64 s[0:1], s[0:1], s[28:29]
	v_cmp_gt_i32_e64 s[24:25], 49, v213
	v_cndmask_b32_e64 v109, v109, v210, s[0:1]
	s_and_b64 s[0:1], s[0:1], s[26:27]
	v_cmp_gt_i32_e64 s[22:23], 48, v213
	v_cndmask_b32_e64 v108, v108, v210, s[0:1]
	s_and_b64 s[0:1], s[0:1], s[24:25]
	v_cmp_gt_i32_e64 s[20:21], 43, v213
	v_cndmask_b32_e64 v107, v107, v210, s[0:1]
	s_and_b64 s[0:1], s[0:1], s[22:23]
	v_cmp_gt_i32_e64 s[18:19], 42, v213
	v_cndmask_b32_e64 v106, v106, v210, s[0:1]
	s_and_b64 s[0:1], s[0:1], s[20:21]
	v_cmp_gt_i32_e64 s[16:17], 41, v213
	v_cndmask_b32_e64 v105, v105, v210, s[0:1]
	s_and_b64 s[0:1], s[0:1], s[18:19]
	v_cmp_gt_i32_e64 s[14:15], 40, v213
	v_cndmask_b32_e64 v104, v104, v210, s[0:1]
	s_and_b64 s[0:1], s[0:1], s[16:17]
	v_cmp_gt_i32_e64 s[12:13], 35, v213
	v_cndmask_b32_e64 v103, v103, v210, s[0:1]
	s_and_b64 s[0:1], s[0:1], s[14:15]
	v_cmp_gt_i32_e64 s[10:11], 34, v213
	v_cndmask_b32_e64 v102, v102, v210, s[0:1]
	s_and_b64 s[0:1], s[0:1], s[12:13]
	v_cmp_gt_i32_e64 s[8:9], 33, v213
	v_cndmask_b32_e64 v101, v101, v210, s[0:1]
	s_and_b64 s[0:1], s[0:1], s[10:11]
	v_cmp_gt_i32_e32 vcc, 32, v213
	v_cndmask_b32_e64 v100, v100, v210, s[0:1]
	s_and_b64 s[0:1], s[0:1], s[8:9]
	s_and_b64 vcc, s[0:1], vcc
	v_cndmask_b32_e64 v97, v97, v210, s[68:69]
	v_cndmask_b32_e64 v96, v96, v210, s[66:67]
	v_cndmask_b32_e64 v95, v95, v210, s[64:65]
	v_cndmask_b32_e64 v94, v94, v210, s[62:63]
	v_cndmask_b32_e64 v93, v93, v210, s[60:61]
	v_cndmask_b32_e64 v92, v92, v210, s[58:59]
	v_cndmask_b32_e64 v91, v91, v210, s[56:57]
	v_cndmask_b32_e64 v90, v90, v210, s[54:55]
	v_cndmask_b32_e64 v89, v89, v210, s[52:53]
	v_cndmask_b32_e64 v88, v88, v210, s[50:51]
	v_cndmask_b32_e64 v87, v87, v210, s[48:49]
	v_cndmask_b32_e64 v86, v86, v210, s[46:47]
	v_cndmask_b32_e64 v85, v85, v210, s[44:45]
	v_cndmask_b32_e64 v84, v84, v210, s[42:43]
	v_cndmask_b32_e64 v83, v83, v210, s[38:39]
	v_cndmask_b32_e64 v99, v99, v210, s[0:1]
	v_cndmask_b32_e32 v98, v98, v210, vcc

; template <bool MLA>
; __device__ __forceinline__ void attn_unit(const P& p, LAS unsigned char* lds, const int b, const int h, const int qb) {
;     ...
;                 l_run = l_run * alpha + ps;
;                 if (__any(alpha < 1.f)) { if (hi == 0) al[r32] = alpha; asm volatile("s_waitcnt lgkmcnt(0)" ::: "memory");
; #pragma unroll
;                     for (int r = 0; r < 16; ++r) { const float a = al[(r & 3) + 8 * (r >> 2) + 4 * hi];
; #pragma unroll
;                         for (int d0 = 0; d0 < 4; ++d0) o[d0][r] *= a; } }
;                 pf0 = packf(p0, 0); pf1 = packf(p0, 1); pf2 = packf(p1, 0); pf3 = packf(p1, 1);
;             } else {
;                 if (k0 + 63 >= qw) {
; #pragma unroll
;                     for (int r = 0; r < 16; ++r) { const int c = (r & 3) + 8 * (r >> 2); if (c >= dq) p0[r] = -__builtin_inff(); if (c + 32 >= dq) p1[r] = -__builtin_inff(); } }
;                 float lsum = 0.f; bf16x8 lf[4];
; #pragma unroll
;                 for (int g = 0; g < 4; ++g) {
;                     float Lv[8];
; #pragma unroll
;                     for (int j = 0; j < 8; ++j) { const int r = 8 * (g & 1) + j;
;                         const float z = (g < 2 ? p0[r] : p1[r]);
;                         const float t = __builtin_amdgcn_logf(1.f + __builtin_amdgcn_exp2f(-fabsf(z)));
;                         const float L = -(fmaxf(z, 0.f) + t);
;                         const float ls = fminf(z, 0.f) - t;
;                         if (g < 2) p0[r] = ls; else p1[r] = ls;
;                         Lv[j] = L; lsum += L; }
;                     u32x4 w; w.x = pk2(Lv[0], Lv[1]); w.y = pk2(Lv[2], Lv[3]); w.z = pk2(Lv[4], Lv[5]); w.w = pk2(Lv[6], Lv[7]); lf[g] = __builtin_bit_cast(bf16x8, w);
;                 }
;                 p0 = AT_MFMA(tri0, lf[0], p0); p0 = AT_MFMA(tri1, lf[1], p0); p0 = AT_MFMA(ones, lf[2], p0); p0 = AT_MFMA(ones, lf[3], p0);
;                 p1 = AT_MFMA(tri0, lf[2], p1); p1 = AT_MFMA(tri1, lf[3], p1);
; #pragma unroll
;                 for (int r = 0; r < 16; ++r) { p0[r] = __builtin_amdgcn_exp2f(p0[r] + R2); p1[r] = __builtin_amdgcn_exp2f(p1[r] + R2); }
;                 lsum += __shfl_xor(lsum, 32);
;                 R2 += lsum;
;                 pf0 = packf(p0, 0); pf1 = packf(p0, 1); pf2 = packf(p1, 0); pf3 = packf(p1, 1);
;             }
;             const LAS unsigned char* vb = kb + KT;
; #pragma unroll
.LBB0_715:
	ds_read_b128 v[108:111], v243 offset:30272
	ds_read_b128 v[220:223], v243 offset:30304
	v_cvt_pk_bf16_f32 v105, v14, v16
	v_cvt_pk_bf16_f32 v104, v10, v12
	v_cvt_pk_bf16_f32 v106, v84, v87
	v_cvt_pk_bf16_f32 v107, v98, v99
	v_cvt_pk_bf16_f32 v216, v83, v86
	v_cvt_pk_bf16_f32 v217, v88, v90
	v_cvt_pk_bf16_f32 v218, v92, v94
	v_cvt_pk_bf16_f32 v219, v101, v102
	v_cvt_pk_bf16_f32 v4, v4, v5
	v_cvt_pk_bf16_f32 v5, v6, v7
	v_cvt_pk_bf16_f32 v6, v8, v9
	v_cvt_pk_bf16_f32 v7, v11, v13
	v_cvt_pk_bf16_f32 v12, v15, v17
	v_cvt_pk_bf16_f32 v13, v82, v85
	v_cvt_pk_bf16_f32 v14, v89, v91
	v_cvt_pk_bf16_f32 v15, v93, v95
	s_waitcnt lgkmcnt(7)
	v_mfma_f32_32x32x16_bf16 v[66:81], v[104:107], v[228:231], v[66:81]
	ds_read_b128 v[228:231], v243 offset:34816
	s_waitcnt lgkmcnt(7)
	v_mfma_f32_32x32x16_bf16 v[66:81], v[216:219], v[232:235], v[66:81]
	ds_read_b128 v[232:235], v243 offset:34848
	s_waitcnt lgkmcnt(7)
	v_mfma_f32_32x32x16_bf16 v[66:81], v[4:7], v[236:239], v[66:81]
	ds_read_b128 v[236:239], v243 offset:34880
	s_waitcnt lgkmcnt(7)
	v_mfma_f32_32x32x16_bf16 v[66:81], v[12:15], v[244:247], v[66:81]
	ds_read_b128 v[244:247], v243 offset:34912
	s_waitcnt lgkmcnt(7)
	v_mfma_f32_32x32x16_bf16 v[50:65], v[104:107], v[248:251], v[50:65]
	ds_read_b128 v[248:251], v243 offset:39424
	s_waitcnt lgkmcnt(7)
	v_mfma_f32_32x32x16_bf16 v[50:65], v[216:219], v[252:255], v[50:65]
	ds_read_b128 v[252:255], v243 offset:39456
	s_waitcnt lgkmcnt(7)
	v_mfma_f32_32x32x16_bf16 v[50:65], v[4:7], v[108:111], v[50:65]
	ds_read_b128 v[108:111], v243 offset:39488
	s_waitcnt lgkmcnt(7)
	v_mfma_f32_32x32x16_bf16 v[50:65], v[12:15], v[220:223], v[50:65]
	ds_read_b128 v[220:223], v243 offset:39520
	s_waitcnt lgkmcnt(7)
	v_mfma_f32_32x32x16_bf16 v[34:49], v[104:107], v[228:231], v[34:49]
	s_waitcnt lgkmcnt(6)
	v_mfma_f32_32x32x16_bf16 v[34:49], v[216:219], v[232:235], v[34:49]
	s_waitcnt lgkmcnt(5)
	v_mfma_f32_32x32x16_bf16 v[34:49], v[4:7], v[236:239], v[34:49]
	s_waitcnt lgkmcnt(4)
	v_mfma_f32_32x32x16_bf16 v[34:49], v[12:15], v[244:247], v[34:49]
	s_waitcnt lgkmcnt(3)
	v_add_f32_e32 v17, v97, v100
	v_fmac_f32_e32 v17, v215, v96
	v_mfma_f32_32x32x16_bf16 v[18:33], v[104:107], v[248:251], v[18:33]
	s_waitcnt lgkmcnt(2)
	v_mfma_f32_32x32x16_bf16 v[18:33], v[216:219], v[252:255], v[18:33]
	s_waitcnt lgkmcnt(1)
	v_mfma_f32_32x32x16_bf16 v[18:33], v[4:7], v[108:111], v[18:33]
	s_waitcnt lgkmcnt(0)
	v_mfma_f32_32x32x16_bf16 v[18:33], v[12:15], v[220:223], v[18:33]
	v_mov_b32_e32 v215, v17
	s_andn2_b64 vcc, exec, s[86:87]
	s_cbranch_vccz .LBB0_717
	s_branch .LBB0_718

; #define LAS __attribute__((address_space(3)))
; #define AT_MFMA(a, b, c) __builtin_amdgcn_mfma_f32_32x32x16_bf16((a), (b), (c), 0, 0, 0)
; template <bool MLA>
; __device__ __forceinline__ void attn_unit(const P& p, LAS unsigned char* lds, const int b, const int h, const int qb) {
;     ...
;             for (int s = 0; s < NQF; ++s) { const bf16x8 a0 = *(const LAS bf16x8*)(kb + r32 * KSTR + s * 32 + hi * 16), a1 = *(const LAS bf16x8*)(kb + (32 + r32) * KSTR + s * 32 + hi * 16);
;                 p0 = AT_MFMA(a0, qf[s], p0); p1 = AT_MFMA(a1, qf[s], p1); if ((s & 3) == 3) __builtin_amdgcn_sched_barrier(0); }
;     ...
;             for (int d0 = 0; d0 < 4; ++d0) { const LAS unsigned char* vr = vb + (32 * d0 + r32) * VSTR + hi * 16;
;                 o[d0] = AT_MFMA(pf0, *(const LAS bf16x8*)(vr), o[d0]); o[d0] = AT_MFMA(pf1, *(const LAS bf16x8*)(vr + 32), o[d0]);
;                 o[d0] = AT_MFMA(pf2, *(const LAS bf16x8*)(vr + 64), o[d0]); o[d0] = AT_MFMA(pf3, *(const LAS bf16x8*)(vr + 96), o[d0]); __builtin_amdgcn_sched_barrier(0); }
.LBB0_874:
	s_and_b32 s95, s0, 1
	s_sub_i32 s0, s84, 64
	s_cmp_gt_u32 s0, s93
	s_cbranch_scc1 .LBB0_882
	s_mul_i32 s0, s95, 0xac00
	s_add_i32 s96, s0, 0
	v_add3_u32 v3, s96, v205, v201
	ds_read_b128 v[4:7], v3
	ds_read_b128 v[8:11], v3 offset:12800
	ds_read_b128 v[12:15], v3 offset:32
	ds_read_b128 v[228:231], v3 offset:12832
	ds_read_b128 v[232:235], v3 offset:64
	ds_read_b128 v[236:239], v3 offset:12864
	ds_read_b128 v[244:247], v3 offset:96
	ds_read_b128 v[248:251], v3 offset:12896
	s_waitcnt lgkmcnt(7)
	v_mfma_f32_32x32x16_bf16 v[82:97], v[4:7], v[134:137], 0
	ds_read_b128 v[252:255], v3 offset:128
	s_waitcnt lgkmcnt(7)
	v_mfma_f32_32x32x16_bf16 v[98:113], v[8:11], v[134:137], 0
	ds_read_b128 v[4:7], v3 offset:12928
	s_waitcnt lgkmcnt(7)
	v_mfma_f32_32x32x16_bf16 v[82:97], v[12:15], v[114:117], v[82:97]
	ds_read_b128 v[8:11], v3 offset:160
	s_waitcnt lgkmcnt(7)
	v_mfma_f32_32x32x16_bf16 v[98:113], v[228:231], v[114:117], v[98:113]
	ds_read_b128 v[12:15], v3 offset:12960
	s_waitcnt lgkmcnt(7)
	v_mfma_f32_32x32x16_bf16 v[82:97], v[232:235], v[118:121], v[82:97]
	ds_read_b128 v[228:231], v3 offset:192
	s_waitcnt lgkmcnt(7)
	v_mfma_f32_32x32x16_bf16 v[98:113], v[236:239], v[118:121], v[98:113]
	ds_read_b128 v[232:235], v3 offset:12992
	s_waitcnt lgkmcnt(7)
	v_mfma_f32_32x32x16_bf16 v[82:97], v[244:247], v[122:125], v[82:97]
	ds_read_b128 v[236:239], v3 offset:224
	s_waitcnt lgkmcnt(7)
	v_mfma_f32_32x32x16_bf16 v[98:113], v[248:251], v[122:125], v[98:113]
	ds_read_b128 v[244:247], v3 offset:13024
	s_waitcnt lgkmcnt(7)
	v_mfma_f32_32x32x16_bf16 v[82:97], v[252:255], v[126:129], v[82:97]
	ds_read_b128 v[248:251], v3 offset:256
	s_waitcnt lgkmcnt(7)
	v_mfma_f32_32x32x16_bf16 v[98:113], v[4:7], v[126:129], v[98:113]
	ds_read_b128 v[252:255], v3 offset:13056
	s_waitcnt lgkmcnt(7)
	v_mfma_f32_32x32x16_bf16 v[82:97], v[8:11], v[146:149], v[82:97]
	ds_read_b128 v[4:7], v3 offset:288
	s_waitcnt lgkmcnt(7)
	v_mfma_f32_32x32x16_bf16 v[98:113], v[12:15], v[146:149], v[98:113]
	ds_read_b128 v[8:11], v3 offset:13088
	s_waitcnt lgkmcnt(7)
	v_mfma_f32_32x32x16_bf16 v[82:97], v[228:231], v[150:153], v[82:97]
	ds_read_b128 v[12:15], v3 offset:320
	s_waitcnt lgkmcnt(7)
	v_mfma_f32_32x32x16_bf16 v[98:113], v[232:235], v[150:153], v[98:113]
	ds_read_b128 v[228:231], v3 offset:13120
	s_waitcnt lgkmcnt(7)
	v_mfma_f32_32x32x16_bf16 v[82:97], v[236:239], v[154:157], v[82:97]
	ds_read_b128 v[232:235], v3 offset:352
	s_waitcnt lgkmcnt(7)
	v_mfma_f32_32x32x16_bf16 v[98:113], v[244:247], v[154:157], v[98:113]
	ds_read_b128 v[236:239], v3 offset:13152
	s_waitcnt lgkmcnt(7)
	v_mfma_f32_32x32x16_bf16 v[82:97], v[248:251], v[158:161], v[82:97]
	s_waitcnt lgkmcnt(6)
	v_mfma_f32_32x32x16_bf16 v[98:113], v[252:255], v[158:161], v[98:113]
	s_waitcnt lgkmcnt(5)
	v_mfma_f32_32x32x16_bf16 v[82:97], v[4:7], v[162:165], v[82:97]
	s_waitcnt lgkmcnt(4)
	v_mfma_f32_32x32x16_bf16 v[98:113], v[8:11], v[162:165], v[98:113]
	s_waitcnt lgkmcnt(3)
	v_mfma_f32_32x32x16_bf16 v[82:97], v[12:15], v[166:169], v[82:97]
	s_waitcnt lgkmcnt(2)
	v_mfma_f32_32x32x16_bf16 v[98:113], v[228:231], v[166:169], v[98:113]
	s_waitcnt lgkmcnt(1)
	v_mfma_f32_32x32x16_bf16 v[82:97], v[232:235], v[130:133], v[82:97]
	s_waitcnt lgkmcnt(0)
	v_mfma_f32_32x32x16_bf16 v[98:113], v[236:239], v[130:133], v[98:113]
	v_add3_u32 v243, s96, v201, v207
	ds_read_b128 v[228:231], v243 offset:25600
	ds_read_b128 v[232:235], v243 offset:25632
	ds_read_b128 v[236:239], v243 offset:25664
	ds_read_b128 v[244:247], v243 offset:25696
	ds_read_b128 v[248:251], v243 offset:30208
	ds_read_b128 v[252:255], v243 offset:30240
	s_add_i32 s0, s84, -1
	s_cmp_le_u32 s0, s2
	s_cbranch_scc1 .LBB0_877
; template <bool MLA>
; __device__ __forceinline__ void attn_unit(const P& p, LAS unsigned char* lds, const int b, const int h, const int qb) {
;     ...
;                 if (k0 + 63 > qw) {
; #pragma unroll
;                     for (int r = 0; r < 16; ++r) { const int c = (r & 3) + 8 * (r >> 2);
;                         if (c > dq) p0[r] = -__builtin_inff(); if (c + 32 > dq) p1[r] = -__builtin_inff(); }
	v_cmp_gt_i32_e64 s[66:67], 26, v216
	v_cmp_gt_i32_e64 s[68:69], 27, v216
	v_cmp_gt_i32_e64 s[64:65], 25, v216
	s_and_b64 s[66:67], s[68:69], s[66:67]
	v_cmp_gt_i32_e64 s[62:63], 24, v216
	s_and_b64 s[64:65], s[66:67], s[64:65]
	v_cmp_gt_i32_e64 s[60:61], 19, v216
	s_and_b64 s[62:63], s[64:65], s[62:63]
	v_cmp_gt_i32_e64 s[58:59], 18, v216
	s_and_b64 s[60:61], s[62:63], s[60:61]
	v_cmp_gt_i32_e64 s[56:57], 17, v216
	s_and_b64 s[58:59], s[60:61], s[58:59]
	v_cmp_gt_i32_e64 s[54:55], 16, v216
	s_and_b64 s[56:57], s[58:59], s[56:57]
	v_cmp_gt_i32_e64 s[52:53], 11, v216
	s_and_b64 s[54:55], s[56:57], s[54:55]
	v_cmp_gt_i32_e64 s[50:51], 10, v216
	s_and_b64 s[52:53], s[54:55], s[52:53]
	v_cmp_gt_i32_e64 s[48:49], 9, v216
	s_and_b64 s[50:51], s[52:53], s[50:51]
	v_cmp_gt_i32_e64 s[46:47], 8, v216
	s_and_b64 s[48:49], s[50:51], s[48:49]
	v_cmp_gt_i32_e64 s[44:45], 3, v216
	s_and_b64 s[46:47], s[48:49], s[46:47]
	v_cmp_gt_i32_e64 s[42:43], 2, v216
	s_and_b64 s[44:45], s[46:47], s[44:45]
	v_cmp_gt_i32_e64 s[38:39], 1, v216
	s_and_b64 s[42:43], s[44:45], s[42:43]
	v_cmp_gt_i32_e64 s[0:1], 0, v216
	s_and_b64 s[38:39], s[42:43], s[38:39]
	s_and_b64 s[0:1], s[38:39], s[0:1]
	v_cmp_gt_i32_e64 s[36:37], 58, v216
	v_cndmask_b32_e64 v82, v82, v213, s[0:1]
	v_cmp_gt_i32_e64 s[0:1], 59, v216
	v_cmp_gt_i32_e64 s[34:35], 57, v216
	v_cmp_gt_i32_e64 s[30:31], 56, v216
	v_cndmask_b32_e64 v113, v113, v213, s[0:1]
	s_and_b64 s[0:1], s[0:1], s[36:37]
	v_cndmask_b32_e64 v112, v112, v213, s[0:1]
	s_and_b64 s[0:1], s[0:1], s[34:35]
	v_cmp_gt_i32_e64 s[28:29], 51, v216
	v_cndmask_b32_e64 v111, v111, v213, s[0:1]
	s_and_b64 s[0:1], s[0:1], s[30:31]
	v_cmp_gt_i32_e64 s[26:27], 50, v216
	v_cndmask_b32_e64 v110, v110, v213, s[0:1]
	s_and_b64 s[0:1], s[0:1], s[28:29]
	v_cmp_gt_i32_e64 s[24:25], 49, v216
	v_cndmask_b32_e64 v109, v109, v213, s[0:1]
	s_and_b64 s[0:1], s[0:1], s[26:27]
	v_cmp_gt_i32_e64 s[22:23], 48, v216
	v_cndmask_b32_e64 v108, v108, v213, s[0:1]
	s_and_b64 s[0:1], s[0:1], s[24:25]
	v_cmp_gt_i32_e64 s[20:21], 43, v216
	v_cndmask_b32_e64 v107, v107, v213, s[0:1]
	s_and_b64 s[0:1], s[0:1], s[22:23]
	v_cmp_gt_i32_e64 s[18:19], 42, v216
	v_cndmask_b32_e64 v106, v106, v213, s[0:1]
	s_and_b64 s[0:1], s[0:1], s[20:21]
	v_cmp_gt_i32_e64 s[16:17], 41, v216
	v_cndmask_b32_e64 v105, v105, v213, s[0:1]
	s_and_b64 s[0:1], s[0:1], s[18:19]
	v_cmp_gt_i32_e64 s[14:15], 40, v216
	v_cndmask_b32_e64 v104, v104, v213, s[0:1]
	s_and_b64 s[0:1], s[0:1], s[16:17]
	v_cmp_gt_i32_e64 s[12:13], 35, v216
	v_cndmask_b32_e64 v103, v103, v213, s[0:1]
	s_and_b64 s[0:1], s[0:1], s[14:15]
	v_cmp_gt_i32_e64 s[10:11], 34, v216
	v_cndmask_b32_e64 v102, v102, v213, s[0:1]
	s_and_b64 s[0:1], s[0:1], s[12:13]
	v_cmp_gt_i32_e64 s[8:9], 33, v216
	v_cndmask_b32_e64 v101, v101, v213, s[0:1]
	s_and_b64 s[0:1], s[0:1], s[10:11]
	v_cmp_gt_i32_e32 vcc, 32, v216
	v_cndmask_b32_e64 v100, v100, v213, s[0:1]
	s_and_b64 s[0:1], s[0:1], s[8:9]
	s_and_b64 vcc, s[0:1], vcc
	v_cndmask_b32_e64 v97, v97, v213, s[68:69]
	v_cndmask_b32_e64 v96, v96, v213, s[66:67]
	v_cndmask_b32_e64 v95, v95, v213, s[64:65]
	v_cndmask_b32_e64 v94, v94, v213, s[62:63]
	v_cndmask_b32_e64 v93, v93, v213, s[60:61]
	v_cndmask_b32_e64 v92, v92, v213, s[58:59]
	v_cndmask_b32_e64 v91, v91, v213, s[56:57]
	v_cndmask_b32_e64 v90, v90, v213, s[54:55]
	v_cndmask_b32_e64 v89, v89, v213, s[52:53]
	v_cndmask_b32_e64 v88, v88, v213, s[50:51]
	v_cndmask_b32_e64 v87, v87, v213, s[48:49]
	v_cndmask_b32_e64 v86, v86, v213, s[46:47]
	v_cndmask_b32_e64 v85, v85, v213, s[44:45]
	v_cndmask_b32_e64 v84, v84, v213, s[42:43]
	v_cndmask_b32_e64 v83, v83, v213, s[38:39]
	v_cndmask_b32_e64 v99, v99, v213, s[0:1]
	v_cndmask_b32_e32 v98, v98, v213, vcc

; template <bool MLA>
; __device__ __forceinline__ void attn_unit(const P& p, LAS unsigned char* lds, const int b, const int h, const int qb) {
;     ...
;                 l_run = l_run * alpha + ps;
;                 if (__any(alpha < 1.f)) { if (hi == 0) al[r32] = alpha; asm volatile("s_waitcnt lgkmcnt(0)" ::: "memory");
; #pragma unroll
;                     for (int r = 0; r < 16; ++r) { const float a = al[(r & 3) + 8 * (r >> 2) + 4 * hi];
; #pragma unroll
;                         for (int d0 = 0; d0 < 4; ++d0) o[d0][r] *= a; } }
;                 pf0 = packf(p0, 0); pf1 = packf(p0, 1); pf2 = packf(p1, 0); pf3 = packf(p1, 1);
;             } else {
;                 if (k0 + 63 >= qw) {
; #pragma unroll
;                     for (int r = 0; r < 16; ++r) { const int c = (r & 3) + 8 * (r >> 2); if (c >= dq) p0[r] = -__builtin_inff(); if (c + 32 >= dq) p1[r] = -__builtin_inff(); } }
;                 float lsum = 0.f; bf16x8 lf[4];
; #pragma unroll
;                 for (int g = 0; g < 4; ++g) {
;                     float Lv[8];
; #pragma unroll
;                     for (int j = 0; j < 8; ++j) { const int r = 8 * (g & 1) + j;
;                         const float z = (g < 2 ? p0[r] : p1[r]);
;                         const float t = __builtin_amdgcn_logf(1.f + __builtin_amdgcn_exp2f(-fabsf(z)));
;                         const float L = -(fmaxf(z, 0.f) + t);
;                         const float ls = fminf(z, 0.f) - t;
;                         if (g < 2) p0[r] = ls; else p1[r] = ls;
;                         Lv[j] = L; lsum += L; }
;                     u32x4 w; w.x = pk2(Lv[0], Lv[1]); w.y = pk2(Lv[2], Lv[3]); w.z = pk2(Lv[4], Lv[5]); w.w = pk2(Lv[6], Lv[7]); lf[g] = __builtin_bit_cast(bf16x8, w);
;                 }
;                 p0 = AT_MFMA(tri0, lf[0], p0); p0 = AT_MFMA(tri1, lf[1], p0); p0 = AT_MFMA(ones, lf[2], p0); p0 = AT_MFMA(ones, lf[3], p0);
;                 p1 = AT_MFMA(tri0, lf[2], p1); p1 = AT_MFMA(tri1, lf[3], p1);
; #pragma unroll
;                 for (int r = 0; r < 16; ++r) { p0[r] = __builtin_amdgcn_exp2f(p0[r] + R2); p1[r] = __builtin_amdgcn_exp2f(p1[r] + R2); }
;                 lsum += __shfl_xor(lsum, 32);
;                 R2 += lsum;
;                 pf0 = packf(p0, 0); pf1 = packf(p0, 1); pf2 = packf(p1, 0); pf3 = packf(p1, 1);
;             }
;             const LAS unsigned char* vb = kb + KT;
; #pragma unroll
.LBB0_881:
	ds_read_b128 v[108:111], v243 offset:30272
	ds_read_b128 v[220:223], v243 offset:30304
	v_cvt_pk_bf16_f32 v105, v14, v16
	v_cvt_pk_bf16_f32 v104, v10, v12
	v_cvt_pk_bf16_f32 v106, v84, v87
	v_cvt_pk_bf16_f32 v107, v98, v99
	v_cvt_pk_bf16_f32 v220, v83, v86
	v_cvt_pk_bf16_f32 v221, v88, v90
	v_cvt_pk_bf16_f32 v222, v92, v94
	v_cvt_pk_bf16_f32 v223, v101, v102
	v_cvt_pk_bf16_f32 v4, v4, v5
	v_cvt_pk_bf16_f32 v5, v6, v7
	v_cvt_pk_bf16_f32 v6, v8, v9
	v_cvt_pk_bf16_f32 v7, v11, v13
	v_cvt_pk_bf16_f32 v12, v15, v17
	v_cvt_pk_bf16_f32 v13, v82, v85
	v_cvt_pk_bf16_f32 v14, v89, v91
	v_cvt_pk_bf16_f32 v15, v93, v95
	s_waitcnt lgkmcnt(7)
	v_mfma_f32_32x32x16_bf16 v[66:81], v[104:107], v[228:231], v[66:81]
	ds_read_b128 v[228:231], v243 offset:34816
	s_waitcnt lgkmcnt(7)
	v_mfma_f32_32x32x16_bf16 v[66:81], v[220:223], v[232:235], v[66:81]
	ds_read_b128 v[232:235], v243 offset:34848
	s_waitcnt lgkmcnt(7)
	v_mfma_f32_32x32x16_bf16 v[66:81], v[4:7], v[236:239], v[66:81]
	ds_read_b128 v[236:239], v243 offset:34880
	s_waitcnt lgkmcnt(7)
	v_mfma_f32_32x32x16_bf16 v[66:81], v[12:15], v[244:247], v[66:81]
	ds_read_b128 v[244:247], v243 offset:34912
	s_waitcnt lgkmcnt(7)
	v_mfma_f32_32x32x16_bf16 v[50:65], v[104:107], v[248:251], v[50:65]
	ds_read_b128 v[248:251], v243 offset:39424
	s_waitcnt lgkmcnt(7)
	v_mfma_f32_32x32x16_bf16 v[50:65], v[220:223], v[252:255], v[50:65]
	ds_read_b128 v[252:255], v243 offset:39456
	s_waitcnt lgkmcnt(7)
	v_mfma_f32_32x32x16_bf16 v[50:65], v[4:7], v[108:111], v[50:65]
	ds_read_b128 v[108:111], v243 offset:39488
	s_waitcnt lgkmcnt(7)
	v_mfma_f32_32x32x16_bf16 v[50:65], v[12:15], v[220:223], v[50:65]
	ds_read_b128 v[220:223], v243 offset:39520
	s_waitcnt lgkmcnt(7)
	v_mfma_f32_32x32x16_bf16 v[34:49], v[104:107], v[228:231], v[34:49]
	s_waitcnt lgkmcnt(6)
	v_mfma_f32_32x32x16_bf16 v[34:49], v[220:223], v[232:235], v[34:49]
	s_waitcnt lgkmcnt(5)
	v_mfma_f32_32x32x16_bf16 v[34:49], v[4:7], v[236:239], v[34:49]
	s_waitcnt lgkmcnt(4)
	v_mfma_f32_32x32x16_bf16 v[34:49], v[12:15], v[244:247], v[34:49]
	s_waitcnt lgkmcnt(3)
	v_add_f32_e32 v17, v97, v100
	v_fmac_f32_e32 v17, v218, v96
	v_mfma_f32_32x32x16_bf16 v[18:33], v[104:107], v[248:251], v[18:33]
	s_waitcnt lgkmcnt(2)
	v_mfma_f32_32x32x16_bf16 v[18:33], v[220:223], v[252:255], v[18:33]
	s_waitcnt lgkmcnt(1)
	v_mfma_f32_32x32x16_bf16 v[18:33], v[4:7], v[108:111], v[18:33]
	s_waitcnt lgkmcnt(0)
	v_mfma_f32_32x32x16_bf16 v[18:33], v[12:15], v[220:223], v[18:33]
	v_mov_b32_e32 v218, v17
	s_andn2_b64 vcc, exec, s[86:87]
	s_cbranch_vccz .LBB0_883
	s_branch .LBB0_884
